# RTO unit head: 12 Q/K/V staging loads issued back to back (plus rtp + RTO tail batching)
# baseline (speedup 1.0000x reference)
.LBB0_732:
	s_bfe_u32 s15, s8, 0x20003
	s_lshl_b32 s2, s0, 6
	v_readlane_b32 s0, v254, 62
	s_or_b32 s0, s15, s0
	s_lshl_b64 s[6:7], s[0:1], 2
	s_add_u32 s6, s44, s6
	v_readlane_b32 s0, v254, 61
	s_addc_u32 s7, s45, s7
	s_or_b32 s0, s15, s0
	v_lshlrev_b32_e32 v0, 4, v142
	global_load_dword v144, v97, s[6:7]
	s_lshl_b64 s[6:7], s[0:1], 2
	v_and_b32_e32 v96, 0xf0, v0
	v_mov_b32_e32 v0, 0x7f
	s_add_u32 s6, s44, s6
	v_bitop3_b32 v6, s2, v0, v142 bitop3:0xc8
	v_or_b32_e32 v143, s2, v142
	s_addc_u32 s7, s45, s7
	v_add_u32_e32 v0, s9, v6
	v_mov_b64_e32 v[4:5], s[84:85]
	global_load_dword v145, v97, s[6:7]
	v_mad_i64_i32 v[0:1], s[6:7], v0, s95, v[4:5]
	s_lshl_b32 s0, s15, 8
	s_waitcnt vmcnt(2)
	v_ashrrev_i32_e32 v17, 4, v143
	v_lshl_add_u64 v[0:1], v[0:1], 0, s[0:1]
	s_mov_b64 s[6:7], 0x1400
	v_add_u32_e32 v8, s9, v17
	v_lshl_add_u64 v[0:1], v[0:1], 0, s[6:7]
	v_mad_i64_i32 v[8:9], s[6:7], v8, s95, v[4:5]
	v_lshl_add_u64 v[8:9], v[8:9], 0, s[0:1]
	v_lshl_add_u64 v[12:13], v[8:9], 0, v[96:97]
	s_barrier
	v_bfe_u32 v3, v142, 5, 1
	v_add_u32_e32 v2, 0, v96
	s_movk_i32 s2, 0x110
	v_lshlrev_b32_e32 v6, 1, v6
	v_add_u32_e32 v7, s3, v6
	v_and_b32_e32 v16, 31, v142
	global_load_dwordx4 v[20:23], v[12:13], off offset:3072
	v_add_co_u32_e32 v8, vcc, s63, v12
	s_nop 1
	v_addc_co_u32_e32 v9, vcc, 0, v13, vcc
	global_load_dwordx4 v[24:27], v[8:9], off
	v_mad_u32_u24 v72, v17, s2, v2
	v_and_b32_e32 v8, -8, v17
	v_ashrrev_i32_e32 v9, 31, v8
	v_lshl_add_u64 v[10:11], v[8:9], 1, v[0:1]
	global_load_dwordx4 v[28:31], v[10:11], off
	v_mul_lo_u32 v8, v8, s2
	v_add_u32_e32 v76, v7, v8
	v_add_u32_e32 v8, 0x200, v143
	v_ashrrev_i32_e32 v14, 4, v8
	v_add_u32_e32 v8, s9, v14
	v_mad_i64_i32 v[8:9], s[6:7], v8, s95, v[4:5]
	v_lshl_add_u64 v[8:9], v[8:9], 0, s[0:1]
	v_lshl_add_u64 v[12:13], v[8:9], 0, v[96:97]
	global_load_dwordx4 v[32:35], v[12:13], off offset:3072
	v_add_co_u32_e32 v8, vcc, s63, v12
	s_nop 1
	v_addc_co_u32_e32 v9, vcc, 0, v13, vcc
	global_load_dwordx4 v[36:39], v[8:9], off
	v_mad_u32_u24 v73, v14, s2, v2
	v_and_b32_e32 v8, -8, v14
	v_ashrrev_i32_e32 v9, 31, v8
	v_lshl_add_u64 v[10:11], v[8:9], 1, v[0:1]
	global_load_dwordx4 v[40:43], v[10:11], off
	v_mul_lo_u32 v8, v8, s2
	v_add_u32_e32 v77, v7, v8
	v_add_u32_e32 v8, 0x400, v143
	v_ashrrev_i32_e32 v14, 4, v8
	v_add_u32_e32 v8, s9, v14
	v_mad_i64_i32 v[8:9], s[6:7], v8, s95, v[4:5]
	v_lshl_add_u64 v[8:9], v[8:9], 0, s[0:1]
	v_lshl_add_u64 v[12:13], v[8:9], 0, v[96:97]
	global_load_dwordx4 v[44:47], v[12:13], off offset:3072
	v_add_co_u32_e32 v8, vcc, s63, v12
	s_nop 1
	v_addc_co_u32_e32 v9, vcc, 0, v13, vcc
	global_load_dwordx4 v[48:51], v[8:9], off
	v_mad_u32_u24 v74, v14, s2, v2
	v_and_b32_e32 v8, -8, v14
	v_ashrrev_i32_e32 v9, 31, v8
	v_lshl_add_u64 v[10:11], v[8:9], 1, v[0:1]
	global_load_dwordx4 v[52:55], v[10:11], off
	v_mul_lo_u32 v8, v8, s2
	v_add_u32_e32 v78, v7, v8
	v_add_u32_e32 v8, 0x600, v143
	v_ashrrev_i32_e32 v14, 4, v8
	v_add_u32_e32 v8, s9, v14
	v_mad_i64_i32 v[8:9], s[6:7], v8, s95, v[4:5]
	v_lshl_add_u64 v[8:9], v[8:9], 0, s[0:1]
	v_lshl_add_u64 v[12:13], v[8:9], 0, v[96:97]
	global_load_dwordx4 v[56:59], v[12:13], off offset:3072
	v_add_co_u32_e32 v8, vcc, s63, v12
	s_nop 1
	v_addc_co_u32_e32 v9, vcc, 0, v13, vcc
	global_load_dwordx4 v[60:63], v[8:9], off
	v_mad_u32_u24 v75, v14, s2, v2
	v_and_b32_e32 v8, -8, v14
	v_ashrrev_i32_e32 v9, 31, v8
	v_lshl_add_u64 v[10:11], v[8:9], 1, v[0:1]
	global_load_dwordx4 v[68:71], v[10:11], off
	v_mul_lo_u32 v8, v8, s2
	v_add_u32_e32 v79, v7, v8
	v_lshlrev_b32_e32 v17, 2, v3
	s_movk_i32 s0, 0x60
	v_lshlrev_b32_e32 v96, 4, v3
	v_add_u32_e32 v18, 0, v96
	v_mad_u32_u24 v19, v16, s2, v18
	v_lshrrev_b32_e32 v0, 1, v143
	v_and_or_b32 v146, v0, s0, v16
	v_mad_u32_u24 v0, v146, s2, v18
	s_waitcnt vmcnt(11)
	ds_write_b128 v72, v[20:23]
	s_waitcnt vmcnt(10)
	ds_write_b128 v72, v[24:27] offset:34816
	s_waitcnt vmcnt(9)
	ds_write_b16 v76, v28
	ds_write_b16_d16_hi v76, v28 offset:272
	ds_write_b16 v76, v29 offset:544
	ds_write_b16_d16_hi v76, v29 offset:816
	ds_write_b16 v76, v30 offset:1088
	ds_write_b16_d16_hi v76, v30 offset:1360
	ds_write_b16 v76, v31 offset:1632
	ds_write_b16_d16_hi v76, v31 offset:1904
	s_waitcnt vmcnt(8)
	ds_write_b128 v73, v[32:35]
	s_waitcnt vmcnt(7)
	ds_write_b128 v73, v[36:39] offset:34816
	s_waitcnt vmcnt(6)
	ds_write_b16 v77, v40
	ds_write_b16_d16_hi v77, v40 offset:272
	ds_write_b16 v77, v41 offset:544
	ds_write_b16_d16_hi v77, v41 offset:816
	ds_write_b16 v77, v42 offset:1088
	ds_write_b16_d16_hi v77, v42 offset:1360
	ds_write_b16 v77, v43 offset:1632
	ds_write_b16_d16_hi v77, v43 offset:1904
	s_waitcnt vmcnt(5)
	ds_write_b128 v74, v[44:47]
	s_waitcnt vmcnt(4)
	ds_write_b128 v74, v[48:51] offset:34816
	s_waitcnt vmcnt(3)
	ds_write_b16 v78, v52
	ds_write_b16_d16_hi v78, v52 offset:272
	ds_write_b16 v78, v53 offset:544
	ds_write_b16_d16_hi v78, v53 offset:816
	ds_write_b16 v78, v54 offset:1088
	ds_write_b16_d16_hi v78, v54 offset:1360
	ds_write_b16 v78, v55 offset:1632
	ds_write_b16_d16_hi v78, v55 offset:1904
	s_waitcnt vmcnt(2)
	ds_write_b128 v75, v[56:59]
	s_waitcnt vmcnt(1)
	ds_write_b128 v75, v[60:63] offset:34816
	s_waitcnt vmcnt(0)
	ds_write_b16 v79, v68
	ds_write_b16_d16_hi v79, v68 offset:272
	ds_write_b16 v79, v69 offset:544
	ds_write_b16_d16_hi v79, v69 offset:816
	ds_write_b16 v79, v70 offset:1088
	ds_write_b16_d16_hi v79, v70 offset:1360
	ds_write_b16 v79, v71 offset:1632
	ds_write_b16_d16_hi v79, v71 offset:1904
	s_waitcnt lgkmcnt(0)
	s_barrier
	ds_read_b128 v[64:67], v0
	ds_read_b128 v[106:109], v0 offset:32
	ds_read_b128 v[102:105], v0 offset:64
	ds_read_b128 v[92:95], v0 offset:96
	ds_read_b128 v[88:91], v0 offset:128
	ds_read_b128 v[84:87], v0 offset:160
	ds_read_b128 v[80:83], v0 offset:192
	ds_read_b128 v[98:101], v0 offset:224
	ds_read_b128 v[0:3], v19 offset:34816
	ds_read_b128 v[20:23], v19 offset:34848
	s_waitcnt lgkmcnt(1)
	v_mfma_f32_32x32x16_bf16 v[0:15], v[0:3], v[64:67], 0
	s_waitcnt lgkmcnt(0)
	v_mfma_f32_32x32x16_bf16 v[0:15], v[20:23], v[106:109], v[0:15]
	ds_read_b128 v[20:23], v19 offset:34880
	s_waitcnt lgkmcnt(0)
	v_mfma_f32_32x32x16_bf16 v[0:15], v[20:23], v[102:105], v[0:15]
	ds_read_b128 v[20:23], v19 offset:34912
	s_waitcnt lgkmcnt(0)
	v_mfma_f32_32x32x16_bf16 v[0:15], v[20:23], v[92:95], v[0:15]
	ds_read_b128 v[20:23], v19 offset:34944
	s_waitcnt lgkmcnt(0)
	v_mfma_f32_32x32x16_bf16 v[0:15], v[20:23], v[88:91], v[0:15]
	ds_read_b128 v[20:23], v19 offset:34976
	s_waitcnt lgkmcnt(0)
	v_mfma_f32_32x32x16_bf16 v[0:15], v[20:23], v[84:87], v[0:15]
	ds_read_b128 v[20:23], v19 offset:35008
	s_waitcnt lgkmcnt(0)
	v_mfma_f32_32x32x16_bf16 v[0:15], v[20:23], v[80:83], v[0:15]
	ds_read_b128 v[20:23], v19 offset:35040
	s_waitcnt lgkmcnt(0)
	v_mfma_f32_32x32x16_bf16 v[0:15], v[20:23], v[98:101], v[0:15]
	v_sub_u32_e32 v20, v146, v17
	v_cmp_gt_i32_e32 vcc, 1, v20
	s_and_saveexec_b64 s[6:7], vcc
	s_xor_b64 s[6:7], exec, s[6:7]
	s_cbranch_execz .LBB0_734
	v_sub_u32_e32 v19, 0, v20
	v_cvt_f32_u32_e32 v19, v19
	v_cmp_ne_u32_e32 vcc, v146, v17
	v_mul_f32_e32 v19, v145, v19
	v_exp_f32_e32 v19, v19
	s_nop 0
	v_cndmask_b32_e32 v19, 2.0, v19, vcc
